# P8: bias quads loaded at unit header before the K-loop; gather-index loads kept in flight through the epilogue
# speedup vs baseline: 1.0108x; 1.0108x over previous
; #define PG8_UNI64(p) ((const char*)((((unsigned long long)(unsigned)__builtin_amdgcn_readfirstlane((int)((unsigned long long)(p) >> 32))) << 32) | (unsigned long long)(unsigned)__builtin_amdgcn_readfirstlane((int)(unsigned)(unsigned long long)(p))))
;     __device__ __forceinline__ const char* Abase(const pg8::Unit& u) const { size_t o = WS_R1; if (u.aux == 1) o = WS_R3; return ws + o + (size_t)u.pm * TSF8; }
;     __device__ __forceinline__ const char* Bbase(const pg8::Unit& u) const { size_t o = WS_WIN; if (u.aux == 1) o = WS_WKV; return ws + o + (size_t)u.pn * TSF8; }
;     __device__ __forceinline__ const char* Abase(const pg8::Unit& u) const { if (GATH) return ws + WS_XQ; return ws + WS_H2 + (size_t)u.pm * TSF8; }
; template <class Epi, class Sched, bool F8 = false, bool PF = false, bool I8 = false, int PID = -1>
; __device__ __forceinline__ void gemm_phase(LAS unsigned char* lds, LAS unsigned char* xlds, const int RP, const int RPB, const int nt, const Sched& S, const Epi& E, const int stagger_ticks) {
;     ...
;         cur = nxt; cA = nA; cB = nB; ++ui;
;         has_next = has_nn; nxt = nn;
;         if (has_next) { nA = PG8_UNI64(S.Abase(nxt)); nB = PG8_UNI64(S.Bbase(nxt)); }
;         if (Sched::GATHER) { *nslot = (u32x4){gv[0], gv[1], gv[2], gv[3]}; asm volatile("" ::: "memory"); }
;     __device__ __forceinline__ void operator()(const f32x4 (&acc)[2][2][4][2], const pg8::Unit& u, int wr, int wc, int fr, int fq) const {
;         const int e = u.aux;
;         unsigned char* Ht = ws + WS_H2 + (size_t)u.pm * TSF8;
;         const int hc = u.pn * 128 + wc * 32 + 8 * fq;
;         const f32x4 bg0 = *(const f32x4*)(bgate + e * FF + hc), bg1 = *(const f32x4*)(bgate + e * FF + hc + 4);
;         const f32x4 bu0 = *(const f32x4*)(bup + e * FF + hc), bu1 = *(const f32x4*)(bup + e * FF + hc + 4);
.LBB0_957:
	s_mov_b64 s[26:27], s[8:9]
	s_mov_b64 s[8:9], s[22:23]
	s_add_u32 s23, s26, 0x100
	s_mov_b64 s[2:3], s[20:21]
	s_addc_u32 s63, s27, 0
	s_add_u32 s2, s2, 0x80
	s_mov_b64 s[20:21], s[24:25]
	s_mov_b32 s61, s36
	s_mov_b32 s62, s35
	s_mov_b32 s22, s34
	s_mov_b32 s34, s40
	s_mov_b32 s35, s39
	s_mov_b32 s36, s41
	s_addc_u32 s3, s3, 0
	s_mov_b32 s64, -2
	s_lshl_b32 s98, s62, 7
	v_lshrrev_b32_e32 v230, 1, v0
	v_and_or_b32 v230, v230, 24, s98
	v_or_b32_e32 v230, s45, v230
	v_lshlrev_b32_e32 v230, 2, v230
	s_lshl_b32 s98, s61, 12
	s_add_u32 s100, s84, s98
	s_addc_u32 s101, s85, 0
	s_nop 0
	global_load_dwordx4 v[222:225], v230, s[100:101]
	global_load_dwordx4 v[218:221], v230, s[100:101] offset:16
	s_add_u32 s100, s88, s98
	s_addc_u32 s101, s89, 0
	s_nop 0
	global_load_dwordx4 v[226:229], v230, s[100:101]
	global_load_dwordx4 v[214:217], v230, s[100:101] offset:16
	s_branch .LBB0_959

;     __device__ __forceinline__ void a_offsets(const pg8::Unit& u, const int (&R)[2], const int (&C)[2], int RP, unsigned (&v)[4]) const {
;         if (GATH) { const int base = (u.pm - tpre[u.aux]) * 256, cnt = tpre[40 + u.aux]; const int* lpid = (const int*)(ws + WS_LPID);
; #pragma unroll
;             for (int h = 0; h < 2; ++h)
; #pragma unroll
;                 for (int i = 0; i < 2; ++i) { const int pos = base + h * 128 + R[i]; const int pid = lpid[u.aux * LISTCAP + (pos < cnt ? pos : 0)]; v[h * 2 + i] = (unsigned)((pid >> 2) * RP + C[i] * 2); }
.LBB0_966:
	s_mov_b64 s[10:11], 0
	s_andn2_b64 vcc, exec, s[24:25]
	v_mov_b32_e32 v2, v66
	v_mov_b32_e32 v3, v67
	v_mov_b32_e32 v4, v68
	v_mov_b32_e32 v5, v69
	s_cbranch_vccnz .LBB0_969
	s_lshl_b32 s10, s41, 2
	s_add_i32 s10, s10, 0
	s_add_i32 s10, s10, 0x20400
	v_mov_b32_e32 v2, s10
	ds_read2_b32 v[2:3], v2 offset1:40
	s_lshl_b32 s10, s41, 16
	s_waitcnt lgkmcnt(0)
	v_sub_u32_e32 v2, s40, v2
	v_lshlrev_b32_e32 v2, 8, v2
	v_add_u32_e32 v4, v2, v1
	v_add_u32_e32 v6, v2, v200
	v_cmp_lt_i32_e32 vcc, v4, v3
	v_or_b32_e32 v2, 0x80, v2
	s_nop 0
	v_cndmask_b32_e32 v4, 0, v4, vcc
	v_cmp_lt_i32_e32 vcc, v6, v3
	v_add_u32_e32 v4, s10, v4
	v_ashrrev_i32_e32 v5, 31, v4
	v_cndmask_b32_e32 v6, 0, v6, vcc
	v_add_u32_e32 v6, s10, v6
	v_ashrrev_i32_e32 v7, 31, v6
	v_lshl_add_u64 v[4:5], v[4:5], 2, s[4:5]
	v_lshl_add_u64 v[6:7], v[6:7], 2, s[4:5]
	global_load_dword v209, v[4:5], off
	s_nop 0
	global_load_dword v210, v[6:7], off
	v_add_u32_e32 v4, v2, v1
	v_cmp_lt_i32_e32 vcc, v4, v3
	v_add_u32_e32 v2, v2, v200
	s_nop 0
	v_cndmask_b32_e32 v4, 0, v4, vcc
	v_cmp_lt_i32_e32 vcc, v2, v3
	v_add_u32_e32 v4, s10, v4
	v_ashrrev_i32_e32 v5, 31, v4
	v_cndmask_b32_e32 v2, 0, v2, vcc
	v_add_u32_e32 v2, s10, v2
	v_ashrrev_i32_e32 v3, 31, v2
	v_lshl_add_u64 v[4:5], v[4:5], 2, s[4:5]
	v_lshl_add_u64 v[2:3], v[2:3], 2, s[4:5]
	global_load_dword v211, v[4:5], off
	s_nop 0
	global_load_dword v212, v[2:3], off
	s_mov_b64 s[10:11], -1
	s_branch .LBB0_969

; __device__ __forceinline__ unsigned pk4_fp8(float a, float b, float c, float d) { int w = __builtin_amdgcn_cvt_pk_fp8_f32(a, b, 0, false); w = __builtin_amdgcn_cvt_pk_fp8_f32(c, d, w, true); return (unsigned)w; }
;     __device__ __forceinline__ void operator()(const f32x4 (&acc)[2][2][4][2], const pg8::Unit& u, int wr, int wc, int fr, int fq) const {
;         const int e = u.aux;
;         unsigned char* Ht = ws + WS_H2 + (size_t)u.pm * TSF8;
;         const int hc = u.pn * 128 + wc * 32 + 8 * fq;
;         const f32x4 bg0 = *(const f32x4*)(bgate + e * FF + hc), bg1 = *(const f32x4*)(bgate + e * FF + hc + 4);
;         const f32x4 bu0 = *(const f32x4*)(bup + e * FF + hc), bu1 = *(const f32x4*)(bup + e * FF + hc + 4);
; #pragma unroll
;         for (int ai = 0; ai < 2; ++ai)
; #pragma unroll
;             for (int m = 0; m < 4; ++m) { const int rl = ai * 128 + wr * 64 + m * 16 + fr;
;                 const f32x4 g0 = acc[ai][0][m][0] * (1.0f / 64.0f) + bg0, g1 = acc[ai][0][m][1] * (1.0f / 64.0f) + bg1, u0 = acc[ai][1][m][0] * (1.0f / 64.0f) + bu0, u1 = acc[ai][1][m][1] * (1.0f / 64.0f) + bu1;
;                 const f32x2 h0 = act2((f32x2){g0[0], g0[1]}, (f32x2){u0[0], u0[1]}), h1 = act2((f32x2){g0[2], g0[3]}, (f32x2){u0[2], u0[3]});
;                 const f32x2 h2 = act2((f32x2){g1[0], g1[1]}, (f32x2){u1[0], u1[1]}), h3 = act2((f32x2){g1[2], g1[3]}, (f32x2){u1[2], u1[3]});
;                 *(u32x2*)(Ht + (size_t)rl * FF + hc) = (u32x2){pk4_fp8(h0.x, h0.y, h1.x, h1.y), pk4_fp8(h2.x, h2.y, h3.x, h3.y)}; }
.LBB0_969:
	s_ashr_i32 s23, s22, 31
	s_lshl_b64 s[22:23], s[22:23], 18
	v_mov_b32_e32 v24, v0
	s_add_u32 s22, s46, s22
	s_addc_u32 s23, s47, s23
	s_lshl_b32 s24, s62, 7
	v_lshrrev_b32_e32 v6, 1, v24
	v_and_or_b32 v6, v6, 24, s24
	s_lshl_b32 s24, s61, 10
	s_ashr_i32 s25, s24, 31
	v_or_b32_e32 v22, s45, v6
	s_lshl_b64 s[24:25], s[24:25], 2
	s_add_u32 s26, s84, s24
	v_ashrrev_i32_e32 v23, 31, v22
	s_addc_u32 s27, s85, s25
	v_lshlrev_b64 v[6:7], 2, v[22:23]
	v_lshl_add_u64 v[8:9], s[26:27], 0, v[6:7]
	s_add_u32 s24, s88, s24
	s_addc_u32 s25, s89, s25
	v_lshl_add_u64 v[6:7], s[24:25], 0, v[6:7]
	s_nop 0
	v_and_or_b32 v26, v24, 15, s44
	v_ashrrev_i32_e32 v27, 31, v26
	v_lshlrev_b64 v[32:33], 10, v[26:27]
	v_lshl_add_u64 v[24:25], s[22:23], 0, v[22:23]
	v_lshl_add_u64 v[22:23], v[24:25], 0, v[32:33]
	v_mov_b32_e32 v28, v198
	v_mov_b32_e32 v29, v198
	v_or_b32_e32 v30, 16, v26
	v_pk_fma_f32 v[34:35], v[186:187], s[16:17], v[222:223] op_sel_hi:[1,0,1]
	s_nop 0
	v_med3_f32 v34, v34, s48, v208
	v_med3_f32 v35, v35, s48, v208
	v_pk_mul_f32 v[56:57], v[34:35], s[18:19] op_sel_hi:[1,0]
	v_pk_fma_f32 v[32:33], v[188:189], s[16:17], v[224:225] op_sel_hi:[1,0,1]
	v_exp_f32_e32 v56, v56
	v_exp_f32_e32 v57, v57
	v_pk_fma_f32 v[38:39], v[194:195], s[16:17], v[218:219] op_sel_hi:[1,0,1]
	v_med3_f32 v32, v32, s48, v208
	v_med3_f32 v33, v33, s48, v208
	v_med3_f32 v38, v38, s48, v208
	v_med3_f32 v39, v39, s48, v208
	v_pk_mul_f32 v[58:59], v[32:33], s[18:19] op_sel_hi:[1,0]
	v_pk_mul_f32 v[60:61], v[38:39], s[18:19] op_sel_hi:[1,0]
	v_exp_f32_e32 v58, v58
	v_exp_f32_e32 v59, v59
	v_exp_f32_e32 v60, v60
	v_exp_f32_e32 v61, v61
	v_pk_add_f32 v[56:57], v[56:57], 1.0 op_sel_hi:[1,0]
	v_pk_fma_f32 v[36:37], v[196:197], s[16:17], v[220:221] op_sel_hi:[1,0,1]
	v_mul_f32_e32 v27, v56, v57
	v_med3_f32 v36, v36, s48, v208
	v_med3_f32 v37, v37, s48, v208
	v_pk_fma_f32 v[64:65], v[172:173], s[16:17], v[228:229] op_sel_hi:[1,0,1]
	v_rcp_f32_e32 v172, v27
	v_pk_mul_f32 v[62:63], v[36:37], s[18:19] op_sel_hi:[1,0]
	v_pk_add_f32 v[58:59], v[58:59], 1.0 op_sel_hi:[1,0]
	v_exp_f32_e32 v62, v62
	v_exp_f32_e32 v63, v63
	v_pk_add_f32 v[60:61], v[60:61], 1.0 op_sel_hi:[1,0]
	v_pk_fma_f32 v[50:51], v[174:175], s[16:17], v[226:227] op_sel_hi:[1,0,1]
	v_mul_f32_e32 v31, v58, v59
	v_mul_f32_e32 v173, v60, v61
	v_med3_f32 v50, v50, s49, v208
	v_med3_f32 v51, v51, s49, v208
	v_rcp_f32_e32 v174, v31
	v_pk_mul_f32 v[56:57], v[56:57], v[172:173] op_sel:[1,0] op_sel_hi:[0,0]
	v_pk_add_f32 v[50:51], v[50:51], 1.0 op_sel_hi:[1,0]
	v_pk_mul_f32 v[34:35], v[34:35], v[56:57]
	v_pk_add_f32 v[62:63], v[62:63], 1.0 op_sel_hi:[1,0]
	v_pk_mul_f32 v[34:35], v[50:51], v[34:35]
	v_pk_fma_f32 v[48:49], v[176:177], s[16:17], v[228:229] op_sel_hi:[1,0,1]
	v_mul_f32_e32 v175, v62, v63
	v_cvt_pk_fp8_f32 v28, v34, v35
	v_med3_f32 v48, v48, s49, v208
	v_med3_f32 v49, v49, s49, v208
	v_pk_mul_f32 v[58:59], v[58:59], v[174:175] op_sel:[1,0] op_sel_hi:[0,0]
	v_pk_fma_f32 v[42:43], v[190:191], s[16:17], v[222:223] op_sel_hi:[1,0,1]
	v_pk_add_f32 v[48:49], v[48:49], 1.0 op_sel_hi:[1,0]
	v_rcp_f32_e32 v176, v173
	v_pk_mul_f32 v[32:33], v[32:33], v[58:59]
	v_med3_f32 v42, v42, s48, v208
	v_med3_f32 v43, v43, s48, v208
	v_pk_mul_f32 v[32:33], v[48:49], v[32:33]
	v_pk_fma_f32 v[54:55], v[178:179], s[16:17], v[214:215] op_sel_hi:[1,0,1]
	v_cvt_pk_fp8_f32 v28, v32, v33 op_sel:[0,0,1]
	v_pk_mul_f32 v[32:33], v[42:43], s[18:19] op_sel_hi:[1,0]
	v_rcp_f32_e32 v178, v175
	v_exp_f32_e32 v32, v32
	v_exp_f32_e32 v33, v33
	v_med3_f32 v54, v54, s49, v208
	v_med3_f32 v55, v55, s49, v208
	v_pk_mul_f32 v[60:61], v[60:61], v[176:177] op_sel:[1,0] op_sel_hi:[0,0]
	v_pk_add_f32 v[54:55], v[54:55], 1.0 op_sel_hi:[1,0]
	v_pk_mul_f32 v[38:39], v[38:39], v[60:61]
	v_pk_fma_f32 v[40:41], v[192:193], s[16:17], v[224:225] op_sel_hi:[1,0,1]
	v_pk_fma_f32 v[52:53], v[180:181], s[16:17], v[216:217] op_sel_hi:[1,0,1]
	v_pk_mul_f32 v[38:39], v[54:55], v[38:39]
	v_med3_f32 v52, v52, s49, v208
	v_med3_f32 v53, v53, s49, v208
	v_pk_mul_f32 v[62:63], v[62:63], v[178:179] op_sel:[1,0] op_sel_hi:[0,0]
	v_cvt_pk_fp8_f32 v29, v38, v39
	v_pk_add_f32 v[32:33], v[32:33], 1.0 op_sel_hi:[1,0]
	v_med3_f32 v38, v40, s48, v208
	v_med3_f32 v39, v41, s48, v208
	v_pk_add_f32 v[52:53], v[52:53], 1.0 op_sel_hi:[1,0]
	v_pk_mul_f32 v[36:37], v[36:37], v[62:63]
	v_mul_f32_e32 v27, v32, v33
	v_pk_mul_f32 v[40:41], v[38:39], s[18:19] op_sel_hi:[1,0]
	v_pk_mul_f32 v[34:35], v[52:53], v[36:37]
	v_rcp_f32_e32 v36, v27
	v_exp_f32_e32 v40, v40
	v_exp_f32_e32 v41, v41
	v_pk_fma_f32 v[46:47], v[182:183], s[16:17], v[218:219] op_sel_hi:[1,0,1]
	v_pk_mul_f32 v[32:33], v[32:33], v[36:37] op_sel:[1,0] op_sel_hi:[0,0]
	v_pk_fma_f32 v[170:171], v[170:171], s[16:17], v[226:227] op_sel_hi:[1,0,1]
	v_pk_add_f32 v[36:37], v[40:41], 1.0 op_sel_hi:[1,0]
	v_cvt_pk_fp8_f32 v29, v34, v35 op_sel:[0,0,1]
	v_mul_f32_e32 v27, v36, v37
	v_rcp_f32_e32 v40, v27
	v_med3_f32 v34, v170, s49, v208
	v_med3_f32 v35, v171, s49, v208
	v_pk_add_f32 v[34:35], v[34:35], 1.0 op_sel_hi:[1,0]
	v_pk_mul_f32 v[36:37], v[36:37], v[40:41] op_sel:[1,0] op_sel_hi:[0,0]
	v_pk_mul_f32 v[36:37], v[38:39], v[36:37]
	v_med3_f32 v38, v46, s48, v208
	v_med3_f32 v39, v47, s48, v208
	v_pk_mul_f32 v[40:41], v[38:39], s[18:19] op_sel_hi:[1,0]
	v_pk_mul_f32 v[32:33], v[42:43], v[32:33]
	v_exp_f32_e32 v40, v40
	v_exp_f32_e32 v41, v41
	v_pk_mul_f32 v[32:33], v[34:35], v[32:33]
	v_med3_f32 v34, v64, s49, v208
	v_med3_f32 v35, v65, s49, v208
	v_pk_add_f32 v[34:35], v[34:35], 1.0 op_sel_hi:[1,0]
	v_pk_fma_f32 v[44:45], v[184:185], s[16:17], v[220:221] op_sel_hi:[1,0,1]
	v_pk_mul_f32 v[34:35], v[34:35], v[36:37]
; __device__ __forceinline__ unsigned pk4_fp8(float a, float b, float c, float d) { int w = __builtin_amdgcn_cvt_pk_fp8_f32(a, b, 0, false); w = __builtin_amdgcn_cvt_pk_fp8_f32(c, d, w, true); return (unsigned)w; }
;     __device__ __forceinline__ void operator()(const f32x4 (&acc)[2][2][4][2], const pg8::Unit& u, int wr, int wc, int fr, int fq) const {
;     ...
; #pragma unroll
;         for (int ai = 0; ai < 2; ++ai)
; #pragma unroll
;             for (int m = 0; m < 4; ++m) { const int rl = ai * 128 + wr * 64 + m * 16 + fr;
;                 const f32x4 g0 = acc[ai][0][m][0] * (1.0f / 64.0f) + bg0, g1 = acc[ai][0][m][1] * (1.0f / 64.0f) + bg1, u0 = acc[ai][1][m][0] * (1.0f / 64.0f) + bu0, u1 = acc[ai][1][m][1] * (1.0f / 64.0f) + bu1;
;                 const f32x2 h0 = act2((f32x2){g0[0], g0[1]}, (f32x2){u0[0], u0[1]}), h1 = act2((f32x2){g0[2], g0[3]}, (f32x2){u0[2], u0[3]});
;                 const f32x2 h2 = act2((f32x2){g1[0], g1[1]}, (f32x2){u1[0], u1[1]}), h3 = act2((f32x2){g1[2], g1[3]}, (f32x2){u1[2], u1[3]});
;                 *(u32x2*)(Ht + (size_t)rl * FF + hc) = (u32x2){pk4_fp8(h0.x, h0.y, h1.x, h1.y), pk4_fp8(h2.x, h2.y, h3.x, h3.y)}; }
	v_pk_add_f32 v[36:37], v[40:41], 1.0 op_sel_hi:[1,0]
	v_med3_f32 v42, v44, s48, v208
	v_mul_f32_e32 v27, v36, v37
	v_med3_f32 v43, v45, s48, v208
	v_rcp_f32_e32 v40, v27
	v_pk_mul_f32 v[44:45], v[42:43], s[18:19] op_sel_hi:[1,0]
	global_store_dwordx2 v[22:23], v[28:29], off
	v_exp_f32_e32 v44, v44
	v_exp_f32_e32 v45, v45
	v_pk_mul_f32 v[36:37], v[36:37], v[40:41] op_sel:[1,0] op_sel_hi:[0,0]
	v_pk_mul_f32 v[36:37], v[38:39], v[36:37]
	v_pk_fma_f32 v[28:29], v[166:167], s[16:17], v[214:215] op_sel_hi:[1,0,1]
	v_pk_add_f32 v[38:39], v[44:45], 1.0 op_sel_hi:[1,0]
	v_med3_f32 v28, v28, s49, v208
	v_mul_f32_e32 v27, v38, v39
	v_rcp_f32_e32 v40, v27
	v_med3_f32 v29, v29, s49, v208
	v_pk_add_f32 v[28:29], v[28:29], 1.0 op_sel_hi:[1,0]
	v_pk_fma_f32 v[168:169], v[168:169], s[16:17], v[216:217] op_sel_hi:[1,0,1]
	v_pk_mul_f32 v[38:39], v[38:39], v[40:41] op_sel:[1,0] op_sel_hi:[0,0]
	v_mov_b32_e32 v40, v198
	v_cvt_pk_fp8_f32 v40, v32, v33
	v_pk_fma_f32 v[32:33], v[154:155], s[16:17], v[222:223] op_sel_hi:[1,0,1]
	v_pk_mul_f32 v[28:29], v[28:29], v[36:37]
	v_med3_f32 v32, v32, s48, v208
	v_med3_f32 v33, v33, s48, v208
	v_mov_b32_e32 v41, v198
	v_pk_mul_f32 v[44:45], v[32:33], s[18:19] op_sel_hi:[1,0]
	v_cvt_pk_fp8_f32 v41, v28, v29
	v_exp_f32_e32 v44, v44
	v_exp_f32_e32 v45, v45
	v_med3_f32 v36, v168, s49, v208
	v_med3_f32 v37, v169, s49, v208
	v_pk_add_f32 v[36:37], v[36:37], 1.0 op_sel_hi:[1,0]
	v_pk_mul_f32 v[28:29], v[42:43], v[38:39]
	v_ashrrev_i32_e32 v31, 31, v30
	v_pk_mul_f32 v[28:29], v[36:37], v[28:29]
	v_pk_add_f32 v[44:45], v[44:45], 1.0 op_sel_hi:[1,0]
	v_cvt_pk_fp8_f32 v41, v28, v29 op_sel:[0,0,1]
	v_lshlrev_b64 v[28:29], 10, v[30:31]
	v_pk_fma_f32 v[30:31], v[156:157], s[16:17], v[224:225] op_sel_hi:[1,0,1]
	v_mul_f32_e32 v27, v44, v45
	v_med3_f32 v30, v30, s48, v208
	v_med3_f32 v31, v31, s48, v208
	v_rcp_f32_e32 v48, v27
	v_pk_mul_f32 v[50:51], v[30:31], s[18:19] op_sel_hi:[1,0]
	v_cvt_pk_fp8_f32 v40, v34, v35 op_sel:[0,0,1]
	v_exp_f32_e32 v50, v50
	v_exp_f32_e32 v51, v51
	v_pk_mul_f32 v[44:45], v[44:45], v[48:49] op_sel:[1,0] op_sel_hi:[0,0]
	v_pk_mul_f32 v[32:33], v[32:33], v[44:45]
	v_lshl_add_u64 v[28:29], v[24:25], 0, v[28:29]
	v_pk_add_f32 v[44:45], v[50:51], 1.0 op_sel_hi:[1,0]
	global_store_dwordx2 v[28:29], v[40:41], off
	v_mul_f32_e32 v27, v44, v45
	v_rcp_f32_e32 v48, v27
	v_pk_fma_f32 v[40:41], v[162:163], s[16:17], v[226:227] op_sel_hi:[1,0,1]
	v_pk_fma_f32 v[36:37], v[150:151], s[16:17], v[218:219] op_sel_hi:[1,0,1]
	v_med3_f32 v40, v40, s49, v208
	v_med3_f32 v41, v41, s49, v208
	v_pk_add_f32 v[40:41], v[40:41], 1.0 op_sel_hi:[1,0]
	v_med3_f32 v36, v36, s48, v208
	v_pk_mul_f32 v[32:33], v[40:41], v[32:33]
	v_pk_mul_f32 v[40:41], v[44:45], v[48:49] op_sel:[1,0] op_sel_hi:[0,0]
	v_med3_f32 v37, v37, s48, v208
	v_pk_mul_f32 v[30:31], v[30:31], v[40:41]
	v_pk_mul_f32 v[40:41], v[36:37], s[18:19] op_sel_hi:[1,0]
	v_pk_fma_f32 v[38:39], v[164:165], s[16:17], v[228:229] op_sel_hi:[1,0,1]
	v_exp_f32_e32 v40, v40
	v_exp_f32_e32 v41, v41
	v_pk_fma_f32 v[34:35], v[152:153], s[16:17], v[220:221] op_sel_hi:[1,0,1]
	v_med3_f32 v38, v38, s49, v208
	v_med3_f32 v39, v39, s49, v208
	v_pk_add_f32 v[40:41], v[40:41], 1.0 op_sel_hi:[1,0]
	v_pk_fma_f32 v[46:47], v[158:159], s[16:17], v[214:215] op_sel_hi:[1,0,1]
	v_pk_add_f32 v[38:39], v[38:39], 1.0 op_sel_hi:[1,0]
	v_mul_f32_e32 v27, v40, v41
	v_med3_f32 v34, v34, s48, v208
	v_med3_f32 v35, v35, s48, v208
	v_pk_mul_f32 v[30:31], v[38:39], v[30:31]
	v_med3_f32 v38, v46, s49, v208
	v_med3_f32 v39, v47, s49, v208
	v_rcp_f32_e32 v44, v27
	v_pk_mul_f32 v[46:47], v[34:35], s[18:19] op_sel_hi:[1,0]
	v_pk_fma_f32 v[42:43], v[160:161], s[16:17], v[216:217] op_sel_hi:[1,0,1]
	v_exp_f32_e32 v46, v46
	v_exp_f32_e32 v47, v47
	v_pk_mul_f32 v[40:41], v[40:41], v[44:45] op_sel:[1,0] op_sel_hi:[0,0]
	v_pk_mul_f32 v[36:37], v[36:37], v[40:41]
	v_pk_add_f32 v[38:39], v[38:39], 1.0 op_sel_hi:[1,0]
	v_pk_add_f32 v[40:41], v[46:47], 1.0 op_sel_hi:[1,0]
	v_pk_mul_f32 v[36:37], v[38:39], v[36:37]
	v_mul_f32_e32 v27, v40, v41
	v_rcp_f32_e32 v44, v27
	v_med3_f32 v38, v42, s49, v208
	v_med3_f32 v39, v43, s49, v208
	v_mov_b32_e32 v42, v198
	v_mov_b32_e32 v43, v198
	v_cvt_pk_fp8_f32 v42, v32, v33
	v_cvt_pk_fp8_f32 v43, v36, v37
	v_pk_mul_f32 v[40:41], v[40:41], v[44:45] op_sel:[1,0] op_sel_hi:[0,0]
	v_pk_add_f32 v[38:39], v[38:39], 1.0 op_sel_hi:[1,0]
	v_pk_mul_f32 v[32:33], v[34:35], v[40:41]
	v_or_b32_e32 v28, 32, v26
	v_pk_mul_f32 v[32:33], v[38:39], v[32:33]
	v_cvt_pk_fp8_f32 v42, v30, v31 op_sel:[0,0,1]
	v_cvt_pk_fp8_f32 v43, v32, v33 op_sel:[0,0,1]
	v_ashrrev_i32_e32 v29, 31, v28
	v_lshlrev_b64 v[28:29], 10, v[28:29]
	v_pk_fma_f32 v[30:31], v[138:139], s[16:17], v[222:223] op_sel_hi:[1,0,1]
	v_lshl_add_u64 v[28:29], v[24:25], 0, v[28:29]
	v_med3_f32 v30, v30, s48, v208
	v_med3_f32 v31, v31, s48, v208
	global_store_dwordx2 v[28:29], v[42:43], off
	v_pk_mul_f32 v[42:43], v[30:31], s[18:19] op_sel_hi:[1,0]
	v_pk_fma_f32 v[28:29], v[140:141], s[16:17], v[224:225] op_sel_hi:[1,0,1]
	v_exp_f32_e32 v42, v42
	v_exp_f32_e32 v43, v43
	v_med3_f32 v28, v28, s48, v208
	v_med3_f32 v29, v29, s48, v208
	v_pk_mul_f32 v[48:49], v[28:29], s[18:19] op_sel_hi:[1,0]
	v_pk_add_f32 v[42:43], v[42:43], 1.0 op_sel_hi:[1,0]
	v_exp_f32_e32 v48, v48
	v_mul_f32_e32 v27, v42, v43
	v_rcp_f32_e32 v46, v27
	v_exp_f32_e32 v49, v49
	v_pk_fma_f32 v[38:39], v[146:147], s[16:17], v[226:227] op_sel_hi:[1,0,1]
	v_pk_fma_f32 v[34:35], v[134:135], s[16:17], v[218:219] op_sel_hi:[1,0,1]
	v_pk_mul_f32 v[42:43], v[42:43], v[46:47] op_sel:[1,0] op_sel_hi:[0,0]
	v_pk_mul_f32 v[30:31], v[30:31], v[42:43]
	v_pk_add_f32 v[42:43], v[48:49], 1.0 op_sel_hi:[1,0]
; __device__ __forceinline__ unsigned pk4_fp8(float a, float b, float c, float d) { int w = __builtin_amdgcn_cvt_pk_fp8_f32(a, b, 0, false); w = __builtin_amdgcn_cvt_pk_fp8_f32(c, d, w, true); return (unsigned)w; }
;     __device__ __forceinline__ void operator()(const f32x4 (&acc)[2][2][4][2], const pg8::Unit& u, int wr, int wc, int fr, int fq) const {
;     ...
; #pragma unroll
;         for (int ai = 0; ai < 2; ++ai)
; #pragma unroll
;             for (int m = 0; m < 4; ++m) { const int rl = ai * 128 + wr * 64 + m * 16 + fr;
;                 const f32x4 g0 = acc[ai][0][m][0] * (1.0f / 64.0f) + bg0, g1 = acc[ai][0][m][1] * (1.0f / 64.0f) + bg1, u0 = acc[ai][1][m][0] * (1.0f / 64.0f) + bu0, u1 = acc[ai][1][m][1] * (1.0f / 64.0f) + bu1;
;                 const f32x2 h0 = act2((f32x2){g0[0], g0[1]}, (f32x2){u0[0], u0[1]}), h1 = act2((f32x2){g0[2], g0[3]}, (f32x2){u0[2], u0[3]});
;                 const f32x2 h2 = act2((f32x2){g1[0], g1[1]}, (f32x2){u1[0], u1[1]}), h3 = act2((f32x2){g1[2], g1[3]}, (f32x2){u1[2], u1[3]});
;                 *(u32x2*)(Ht + (size_t)rl * FF + hc) = (u32x2){pk4_fp8(h0.x, h0.y, h1.x, h1.y), pk4_fp8(h2.x, h2.y, h3.x, h3.y)}; }
	v_med3_f32 v38, v38, s49, v208
	v_mul_f32_e32 v27, v42, v43
	v_rcp_f32_e32 v46, v27
	v_med3_f32 v39, v39, s49, v208
	v_pk_add_f32 v[38:39], v[38:39], 1.0 op_sel_hi:[1,0]
	v_med3_f32 v34, v34, s48, v208
	v_pk_mul_f32 v[30:31], v[38:39], v[30:31]
	v_pk_mul_f32 v[38:39], v[42:43], v[46:47] op_sel:[1,0] op_sel_hi:[0,0]
	v_med3_f32 v35, v35, s48, v208
	v_pk_mul_f32 v[28:29], v[28:29], v[38:39]
	v_pk_mul_f32 v[38:39], v[34:35], s[18:19] op_sel_hi:[1,0]
	v_pk_fma_f32 v[36:37], v[148:149], s[16:17], v[228:229] op_sel_hi:[1,0,1]
	v_exp_f32_e32 v38, v38
	v_exp_f32_e32 v39, v39
	v_pk_fma_f32 v[32:33], v[136:137], s[16:17], v[220:221] op_sel_hi:[1,0,1]
	v_med3_f32 v36, v36, s49, v208
	v_med3_f32 v37, v37, s49, v208
	v_pk_add_f32 v[38:39], v[38:39], 1.0 op_sel_hi:[1,0]
	v_pk_fma_f32 v[44:45], v[142:143], s[16:17], v[214:215] op_sel_hi:[1,0,1]
	v_pk_add_f32 v[36:37], v[36:37], 1.0 op_sel_hi:[1,0]
	v_mul_f32_e32 v27, v38, v39
	v_med3_f32 v32, v32, s48, v208
	v_med3_f32 v33, v33, s48, v208
	v_pk_mul_f32 v[28:29], v[36:37], v[28:29]
	v_med3_f32 v36, v44, s49, v208
	v_med3_f32 v37, v45, s49, v208
	v_rcp_f32_e32 v42, v27
	v_pk_mul_f32 v[44:45], v[32:33], s[18:19] op_sel_hi:[1,0]
	v_or_b32_e32 v26, 48, v26
	v_exp_f32_e32 v44, v44
	v_exp_f32_e32 v45, v45
	v_pk_mul_f32 v[38:39], v[38:39], v[42:43] op_sel:[1,0] op_sel_hi:[0,0]
	v_pk_mul_f32 v[34:35], v[34:35], v[38:39]
	v_pk_fma_f32 v[40:41], v[144:145], s[16:17], v[216:217] op_sel_hi:[1,0,1]
	v_pk_add_f32 v[38:39], v[44:45], 1.0 op_sel_hi:[1,0]
	v_pk_add_f32 v[36:37], v[36:37], 1.0 op_sel_hi:[1,0]
	v_mul_f32_e32 v27, v38, v39
	v_rcp_f32_e32 v42, v27
	v_pk_mul_f32 v[34:35], v[36:37], v[34:35]
	v_med3_f32 v36, v40, s49, v208
	v_med3_f32 v37, v41, s49, v208
	v_mov_b32_e32 v40, v198
	v_mov_b32_e32 v41, v198
	v_ashrrev_i32_e32 v27, 31, v26
	v_cvt_pk_fp8_f32 v40, v30, v31
	v_cvt_pk_fp8_f32 v41, v34, v35
	v_lshlrev_b64 v[26:27], 10, v[26:27]
	v_pk_mul_f32 v[38:39], v[38:39], v[42:43] op_sel:[1,0] op_sel_hi:[0,0]
	v_lshl_add_u64 v[24:25], v[24:25], 0, v[26:27]
	v_pk_fma_f32 v[26:27], v[122:123], s[16:17], v[222:223] op_sel_hi:[1,0,1]
	v_pk_add_f32 v[36:37], v[36:37], 1.0 op_sel_hi:[1,0]
	v_pk_mul_f32 v[30:31], v[32:33], v[38:39]
	v_med3_f32 v26, v26, s48, v208
	v_med3_f32 v27, v27, s48, v208
	v_pk_mul_f32 v[30:31], v[36:37], v[30:31]
	v_pk_mul_f32 v[38:39], v[26:27], s[18:19] op_sel_hi:[1,0]
	v_cvt_pk_fp8_f32 v40, v28, v29 op_sel:[0,0,1]
	v_cvt_pk_fp8_f32 v41, v30, v31 op_sel:[0,0,1]
	v_exp_f32_e32 v38, v38
	v_exp_f32_e32 v39, v39
	v_pk_fma_f32 v[34:35], v[130:131], s[16:17], v[226:227] op_sel_hi:[1,0,1]
	global_store_dwordx2 v[24:25], v[40:41], off
	v_pk_fma_f32 v[24:25], v[124:125], s[16:17], v[224:225] op_sel_hi:[1,0,1]
	v_pk_add_f32 v[38:39], v[38:39], 1.0 op_sel_hi:[1,0]
	v_med3_f32 v24, v24, s48, v208
	v_mul_f32_e32 v42, v38, v39
	v_med3_f32 v25, v25, s48, v208
	v_rcp_f32_e32 v42, v42
	v_pk_mul_f32 v[44:45], v[24:25], s[18:19] op_sel_hi:[1,0]
	v_med3_f32 v34, v34, s49, v208
	v_exp_f32_e32 v44, v44
	v_exp_f32_e32 v45, v45
	v_pk_mul_f32 v[38:39], v[38:39], v[42:43] op_sel:[1,0] op_sel_hi:[0,0]
	v_pk_mul_f32 v[26:27], v[26:27], v[38:39]
	v_med3_f32 v35, v35, s49, v208
	v_pk_add_f32 v[38:39], v[44:45], 1.0 op_sel_hi:[1,0]
	v_pk_fma_f32 v[30:31], v[118:119], s[16:17], v[218:219] op_sel_hi:[1,0,1]
	v_mul_f32_e32 v42, v38, v39
	v_rcp_f32_e32 v42, v42
	v_pk_add_f32 v[34:35], v[34:35], 1.0 op_sel_hi:[1,0]
	v_med3_f32 v30, v30, s48, v208
	v_pk_mul_f32 v[26:27], v[34:35], v[26:27]
	v_pk_mul_f32 v[34:35], v[38:39], v[42:43] op_sel:[1,0] op_sel_hi:[0,0]
	v_med3_f32 v31, v31, s48, v208
	v_pk_mul_f32 v[24:25], v[24:25], v[34:35]
	v_pk_mul_f32 v[34:35], v[30:31], s[18:19] op_sel_hi:[1,0]
	v_pk_fma_f32 v[32:33], v[132:133], s[16:17], v[228:229] op_sel_hi:[1,0,1]
	v_exp_f32_e32 v34, v34
	v_exp_f32_e32 v35, v35
	v_pk_fma_f32 v[28:29], v[120:121], s[16:17], v[220:221] op_sel_hi:[1,0,1]
	v_med3_f32 v32, v32, s49, v208
	v_med3_f32 v33, v33, s49, v208
	v_pk_add_f32 v[34:35], v[34:35], 1.0 op_sel_hi:[1,0]
	v_pk_fma_f32 v[40:41], v[126:127], s[16:17], v[214:215] op_sel_hi:[1,0,1]
	v_pk_add_f32 v[32:33], v[32:33], 1.0 op_sel_hi:[1,0]
	v_mul_f32_e32 v38, v34, v35
	v_med3_f32 v28, v28, s48, v208
	v_med3_f32 v29, v29, s48, v208
	v_pk_mul_f32 v[24:25], v[32:33], v[24:25]
	v_med3_f32 v32, v40, s49, v208
	v_med3_f32 v33, v41, s49, v208
	v_rcp_f32_e32 v38, v38
	v_pk_mul_f32 v[40:41], v[28:29], s[18:19] op_sel_hi:[1,0]
	v_pk_fma_f32 v[36:37], v[128:129], s[16:17], v[216:217] op_sel_hi:[1,0,1]
	v_exp_f32_e32 v40, v40
	v_exp_f32_e32 v41, v41
	v_pk_mul_f32 v[34:35], v[34:35], v[38:39] op_sel:[1,0] op_sel_hi:[0,0]
	v_pk_mul_f32 v[30:31], v[30:31], v[34:35]
	v_pk_add_f32 v[32:33], v[32:33], 1.0 op_sel_hi:[1,0]
	v_pk_add_f32 v[34:35], v[40:41], 1.0 op_sel_hi:[1,0]
	v_pk_mul_f32 v[30:31], v[32:33], v[30:31]
	v_mul_f32_e32 v38, v34, v35
	v_rcp_f32_e32 v38, v38
	v_med3_f32 v33, v37, s49, v208
	v_mov_b32_e32 v37, v198
	v_cvt_pk_fp8_f32 v37, v30, v31
	v_med3_f32 v32, v36, s49, v208
	v_pk_mul_f32 v[34:35], v[34:35], v[38:39] op_sel:[1,0] op_sel_hi:[0,0]
	v_mov_b32_e32 v36, v198
	v_pk_add_f32 v[32:33], v[32:33], 1.0 op_sel_hi:[1,0]
	v_cvt_pk_fp8_f32 v36, v26, v27
	v_pk_mul_f32 v[26:27], v[28:29], v[34:35]
	v_pk_fma_f32 v[34:35], v[114:115], s[16:17], v[226:227] op_sel_hi:[1,0,1]
	v_pk_mul_f32 v[26:27], v[32:33], v[26:27]
	v_cvt_pk_fp8_f32 v36, v24, v25 op_sel:[0,0,1]
	v_cvt_pk_fp8_f32 v37, v26, v27 op_sel:[0,0,1]
	v_pk_fma_f32 v[26:27], v[106:107], s[16:17], v[222:223] op_sel_hi:[1,0,1]
	v_add_co_u32_e32 v24, vcc, s50, v22
	v_med3_f32 v26, v26, s48, v208
	v_med3_f32 v27, v27, s48, v208
	v_pk_mul_f32 v[38:39], v[26:27], s[18:19] op_sel_hi:[1,0]
; __device__ __forceinline__ unsigned pk4_fp8(float a, float b, float c, float d) { int w = __builtin_amdgcn_cvt_pk_fp8_f32(a, b, 0, false); w = __builtin_amdgcn_cvt_pk_fp8_f32(c, d, w, true); return (unsigned)w; }
;     __device__ __forceinline__ void operator()(const f32x4 (&acc)[2][2][4][2], const pg8::Unit& u, int wr, int wc, int fr, int fq) const {
;     ...
; #pragma unroll
;         for (int ai = 0; ai < 2; ++ai)
; #pragma unroll
;             for (int m = 0; m < 4; ++m) { const int rl = ai * 128 + wr * 64 + m * 16 + fr;
;                 const f32x4 g0 = acc[ai][0][m][0] * (1.0f / 64.0f) + bg0, g1 = acc[ai][0][m][1] * (1.0f / 64.0f) + bg1, u0 = acc[ai][1][m][0] * (1.0f / 64.0f) + bu0, u1 = acc[ai][1][m][1] * (1.0f / 64.0f) + bu1;
;                 const f32x2 h0 = act2((f32x2){g0[0], g0[1]}, (f32x2){u0[0], u0[1]}), h1 = act2((f32x2){g0[2], g0[3]}, (f32x2){u0[2], u0[3]});
;                 const f32x2 h2 = act2((f32x2){g1[0], g1[1]}, (f32x2){u1[0], u1[1]}), h3 = act2((f32x2){g1[2], g1[3]}, (f32x2){u1[2], u1[3]});
;                 *(u32x2*)(Ht + (size_t)rl * FF + hc) = (u32x2){pk4_fp8(h0.x, h0.y, h1.x, h1.y), pk4_fp8(h2.x, h2.y, h3.x, h3.y)}; }
	v_addc_co_u32_e32 v25, vcc, 0, v23, vcc
	v_exp_f32_e32 v38, v38
	v_exp_f32_e32 v39, v39
	global_store_dwordx2 v[24:25], v[36:37], off
	v_pk_fma_f32 v[24:25], v[108:109], s[16:17], v[224:225] op_sel_hi:[1,0,1]
	v_med3_f32 v34, v34, s49, v208
	v_pk_add_f32 v[38:39], v[38:39], 1.0 op_sel_hi:[1,0]
	v_med3_f32 v24, v24, s48, v208
	v_mul_f32_e32 v42, v38, v39
	v_med3_f32 v25, v25, s48, v208
	v_rcp_f32_e32 v42, v42
	v_pk_mul_f32 v[44:45], v[24:25], s[18:19] op_sel_hi:[1,0]
	v_med3_f32 v35, v35, s49, v208
	v_exp_f32_e32 v44, v44
	v_exp_f32_e32 v45, v45
	v_pk_mul_f32 v[38:39], v[38:39], v[42:43] op_sel:[1,0] op_sel_hi:[0,0]
	v_pk_mul_f32 v[26:27], v[26:27], v[38:39]
	v_pk_fma_f32 v[30:31], v[102:103], s[16:17], v[218:219] op_sel_hi:[1,0,1]
	v_pk_add_f32 v[38:39], v[44:45], 1.0 op_sel_hi:[1,0]
	v_pk_add_f32 v[34:35], v[34:35], 1.0 op_sel_hi:[1,0]
	v_mul_f32_e32 v42, v38, v39
	v_rcp_f32_e32 v42, v42
	v_pk_mul_f32 v[26:27], v[34:35], v[26:27]
	v_med3_f32 v30, v30, s48, v208
	v_med3_f32 v31, v31, s48, v208
	v_pk_mul_f32 v[34:35], v[38:39], v[42:43] op_sel:[1,0] op_sel_hi:[0,0]
	v_pk_mul_f32 v[24:25], v[24:25], v[34:35]
	v_pk_mul_f32 v[34:35], v[30:31], s[18:19] op_sel_hi:[1,0]
	v_pk_fma_f32 v[32:33], v[116:117], s[16:17], v[228:229] op_sel_hi:[1,0,1]
	v_exp_f32_e32 v34, v34
	v_exp_f32_e32 v35, v35
	v_pk_fma_f32 v[28:29], v[104:105], s[16:17], v[220:221] op_sel_hi:[1,0,1]
	v_med3_f32 v32, v32, s49, v208
	v_med3_f32 v33, v33, s49, v208
	v_pk_add_f32 v[34:35], v[34:35], 1.0 op_sel_hi:[1,0]
	v_pk_fma_f32 v[40:41], v[110:111], s[16:17], v[214:215] op_sel_hi:[1,0,1]
	v_pk_add_f32 v[32:33], v[32:33], 1.0 op_sel_hi:[1,0]
	v_mul_f32_e32 v38, v34, v35
	v_med3_f32 v28, v28, s48, v208
	v_med3_f32 v29, v29, s48, v208
	v_pk_mul_f32 v[24:25], v[32:33], v[24:25]
	v_med3_f32 v32, v40, s49, v208
	v_med3_f32 v33, v41, s49, v208
	v_rcp_f32_e32 v38, v38
	v_pk_mul_f32 v[40:41], v[28:29], s[18:19] op_sel_hi:[1,0]
	v_pk_fma_f32 v[36:37], v[112:113], s[16:17], v[216:217] op_sel_hi:[1,0,1]
	v_exp_f32_e32 v40, v40
	v_exp_f32_e32 v41, v41
	v_pk_mul_f32 v[34:35], v[34:35], v[38:39] op_sel:[1,0] op_sel_hi:[0,0]
	v_pk_mul_f32 v[30:31], v[30:31], v[34:35]
	v_pk_add_f32 v[32:33], v[32:33], 1.0 op_sel_hi:[1,0]
	v_pk_add_f32 v[34:35], v[40:41], 1.0 op_sel_hi:[1,0]
	v_pk_mul_f32 v[30:31], v[32:33], v[30:31]
	v_mul_f32_e32 v38, v34, v35
	v_rcp_f32_e32 v38, v38
	v_med3_f32 v33, v37, s49, v208
	v_mov_b32_e32 v37, v198
	v_cvt_pk_fp8_f32 v37, v30, v31
	v_med3_f32 v32, v36, s49, v208
	v_pk_mul_f32 v[34:35], v[34:35], v[38:39] op_sel:[1,0] op_sel_hi:[0,0]
	v_mov_b32_e32 v36, v198
	v_pk_add_f32 v[32:33], v[32:33], 1.0 op_sel_hi:[1,0]
	v_cvt_pk_fp8_f32 v36, v26, v27
	v_pk_mul_f32 v[26:27], v[28:29], v[34:35]
	v_pk_fma_f32 v[34:35], v[98:99], s[16:17], v[226:227] op_sel_hi:[1,0,1]
	v_pk_mul_f32 v[26:27], v[32:33], v[26:27]
	v_cvt_pk_fp8_f32 v36, v24, v25 op_sel:[0,0,1]
	v_cvt_pk_fp8_f32 v37, v26, v27 op_sel:[0,0,1]
	v_pk_fma_f32 v[26:27], v[90:91], s[16:17], v[222:223] op_sel_hi:[1,0,1]
	v_add_co_u32_e32 v24, vcc, s51, v22
	v_med3_f32 v26, v26, s48, v208
	v_med3_f32 v27, v27, s48, v208
	v_pk_mul_f32 v[38:39], v[26:27], s[18:19] op_sel_hi:[1,0]
	v_addc_co_u32_e32 v25, vcc, 0, v23, vcc
	v_exp_f32_e32 v38, v38
	v_exp_f32_e32 v39, v39
	global_store_dwordx2 v[24:25], v[36:37], off
	v_pk_fma_f32 v[24:25], v[92:93], s[16:17], v[224:225] op_sel_hi:[1,0,1]
	v_med3_f32 v34, v34, s49, v208
	v_pk_add_f32 v[38:39], v[38:39], 1.0 op_sel_hi:[1,0]
	v_med3_f32 v24, v24, s48, v208
	v_mul_f32_e32 v42, v38, v39
	v_med3_f32 v25, v25, s48, v208
	v_rcp_f32_e32 v42, v42
	v_pk_mul_f32 v[44:45], v[24:25], s[18:19] op_sel_hi:[1,0]
	v_med3_f32 v35, v35, s49, v208
	v_exp_f32_e32 v44, v44
	v_exp_f32_e32 v45, v45
	v_pk_mul_f32 v[38:39], v[38:39], v[42:43] op_sel:[1,0] op_sel_hi:[0,0]
	v_pk_mul_f32 v[26:27], v[26:27], v[38:39]
	v_pk_fma_f32 v[30:31], v[86:87], s[16:17], v[218:219] op_sel_hi:[1,0,1]
	v_pk_add_f32 v[38:39], v[44:45], 1.0 op_sel_hi:[1,0]
	v_pk_add_f32 v[34:35], v[34:35], 1.0 op_sel_hi:[1,0]
	v_mul_f32_e32 v42, v38, v39
	v_rcp_f32_e32 v42, v42
	v_pk_mul_f32 v[26:27], v[34:35], v[26:27]
	v_med3_f32 v30, v30, s48, v208
	v_med3_f32 v31, v31, s48, v208
	v_pk_mul_f32 v[34:35], v[38:39], v[42:43] op_sel:[1,0] op_sel_hi:[0,0]
	v_pk_mul_f32 v[24:25], v[24:25], v[34:35]
	v_pk_mul_f32 v[34:35], v[30:31], s[18:19] op_sel_hi:[1,0]
	v_pk_fma_f32 v[32:33], v[100:101], s[16:17], v[228:229] op_sel_hi:[1,0,1]
	v_exp_f32_e32 v34, v34
	v_exp_f32_e32 v35, v35
	v_pk_fma_f32 v[28:29], v[88:89], s[16:17], v[220:221] op_sel_hi:[1,0,1]
	v_med3_f32 v32, v32, s49, v208
	v_med3_f32 v33, v33, s49, v208
	v_pk_add_f32 v[34:35], v[34:35], 1.0 op_sel_hi:[1,0]
	v_pk_fma_f32 v[40:41], v[94:95], s[16:17], v[214:215] op_sel_hi:[1,0,1]
	v_pk_add_f32 v[32:33], v[32:33], 1.0 op_sel_hi:[1,0]
	v_mul_f32_e32 v38, v34, v35
	v_med3_f32 v28, v28, s48, v208
	v_med3_f32 v29, v29, s48, v208
	v_pk_mul_f32 v[24:25], v[32:33], v[24:25]
	v_med3_f32 v32, v40, s49, v208
	v_med3_f32 v33, v41, s49, v208
	v_rcp_f32_e32 v38, v38
	v_pk_mul_f32 v[40:41], v[28:29], s[18:19] op_sel_hi:[1,0]
; __device__ __forceinline__ unsigned pk4_fp8(float a, float b, float c, float d) { int w = __builtin_amdgcn_cvt_pk_fp8_f32(a, b, 0, false); w = __builtin_amdgcn_cvt_pk_fp8_f32(c, d, w, true); return (unsigned)w; }
;     __device__ __forceinline__ void a_offsets(const pg8::Unit& u, const int (&R)[2], const int (&C)[2], int RP, unsigned (&v)[4]) const {
;         if (GATH) { const int base = (u.pm - tpre[u.aux]) * 256, cnt = tpre[40 + u.aux]; const int* lpid = (const int*)(ws + WS_LPID);
; #pragma unroll
;             for (int h = 0; h < 2; ++h)
; #pragma unroll
;                 for (int i = 0; i < 2; ++i) { const int pos = base + h * 128 + R[i]; const int pid = lpid[u.aux * LISTCAP + (pos < cnt ? pos : 0)]; v[h * 2 + i] = (unsigned)((pid >> 2) * RP + C[i] * 2); }
;     __device__ __forceinline__ void operator()(const f32x4 (&acc)[2][2][4][2], const pg8::Unit& u, int wr, int wc, int fr, int fq) const {
;     ...
;             for (int m = 0; m < 4; ++m) { const int rl = ai * 128 + wr * 64 + m * 16 + fr;
;                 const f32x4 g0 = acc[ai][0][m][0] * (1.0f / 64.0f) + bg0, g1 = acc[ai][0][m][1] * (1.0f / 64.0f) + bg1, u0 = acc[ai][1][m][0] * (1.0f / 64.0f) + bu0, u1 = acc[ai][1][m][1] * (1.0f / 64.0f) + bu1;
;                 const f32x2 h0 = act2((f32x2){g0[0], g0[1]}, (f32x2){u0[0], u0[1]}), h1 = act2((f32x2){g0[2], g0[3]}, (f32x2){u0[2], u0[3]});
;                 const f32x2 h2 = act2((f32x2){g1[0], g1[1]}, (f32x2){u1[0], u1[1]}), h3 = act2((f32x2){g1[2], g1[3]}, (f32x2){u1[2], u1[3]});
;                 *(u32x2*)(Ht + (size_t)rl * FF + hc) = (u32x2){pk4_fp8(h0.x, h0.y, h1.x, h1.y), pk4_fp8(h2.x, h2.y, h3.x, h3.y)}; }
	v_pk_fma_f32 v[36:37], v[96:97], s[16:17], v[216:217] op_sel_hi:[1,0,1]
	v_exp_f32_e32 v40, v40
	v_exp_f32_e32 v41, v41
	v_pk_mul_f32 v[34:35], v[34:35], v[38:39] op_sel:[1,0] op_sel_hi:[0,0]
	v_pk_mul_f32 v[30:31], v[30:31], v[34:35]
	v_pk_add_f32 v[32:33], v[32:33], 1.0 op_sel_hi:[1,0]
	v_pk_add_f32 v[34:35], v[40:41], 1.0 op_sel_hi:[1,0]
	v_pk_mul_f32 v[30:31], v[32:33], v[30:31]
	v_mul_f32_e32 v38, v34, v35
	v_rcp_f32_e32 v38, v38
	v_med3_f32 v32, v36, s49, v208
	v_med3_f32 v33, v37, s49, v208
	v_mov_b32_e32 v36, v198
	v_mov_b32_e32 v37, v198
	v_cvt_pk_fp8_f32 v36, v26, v27
	v_cvt_pk_fp8_f32 v37, v30, v31
	v_pk_mul_f32 v[34:35], v[34:35], v[38:39] op_sel:[1,0] op_sel_hi:[0,0]
	v_pk_add_f32 v[32:33], v[32:33], 1.0 op_sel_hi:[1,0]
	v_pk_mul_f32 v[26:27], v[28:29], v[34:35]
	v_cvt_pk_fp8_f32 v36, v24, v25 op_sel:[0,0,1]
	v_pk_mul_f32 v[26:27], v[32:33], v[26:27]
	v_add_co_u32_e32 v24, vcc, s60, v22
	v_cvt_pk_fp8_f32 v37, v26, v27 op_sel:[0,0,1]
	v_pk_fma_f32 v[14:15], v[74:75], s[16:17], v[222:223] op_sel_hi:[1,0,1]
	v_addc_co_u32_e32 v25, vcc, 0, v23, vcc
	v_med3_f32 v14, v14, s48, v208
	v_med3_f32 v15, v15, s48, v208
	global_store_dwordx2 v[24:25], v[36:37], off
	v_pk_mul_f32 v[24:25], v[14:15], s[18:19] op_sel_hi:[1,0]
	v_pk_fma_f32 v[16:17], v[76:77], s[16:17], v[224:225] op_sel_hi:[1,0,1]
	v_exp_f32_e32 v24, v24
	v_exp_f32_e32 v25, v25
	v_med3_f32 v16, v16, s48, v208
	v_med3_f32 v17, v17, s48, v208
	v_pk_mul_f32 v[28:29], v[16:17], s[18:19] op_sel_hi:[1,0]
	v_pk_add_f32 v[24:25], v[24:25], 1.0 op_sel_hi:[1,0]
	v_exp_f32_e32 v28, v28
	v_mul_f32_e32 v26, v24, v25
	v_rcp_f32_e32 v26, v26
	v_exp_f32_e32 v29, v29
	v_pk_fma_f32 v[18:19], v[82:83], s[16:17], v[226:227] op_sel_hi:[1,0,1]
	v_pk_fma_f32 v[10:11], v[70:71], s[16:17], v[218:219] op_sel_hi:[1,0,1]
	v_pk_mul_f32 v[24:25], v[24:25], v[26:27] op_sel:[1,0] op_sel_hi:[0,0]
	v_pk_mul_f32 v[14:15], v[14:15], v[24:25]
	v_pk_add_f32 v[24:25], v[28:29], 1.0 op_sel_hi:[1,0]
	v_med3_f32 v18, v18, s49, v208
	v_mul_f32_e32 v26, v24, v25
	v_rcp_f32_e32 v26, v26
	v_med3_f32 v19, v19, s49, v208
	v_pk_fma_f32 v[20:21], v[84:85], s[16:17], v[228:229] op_sel_hi:[1,0,1]
	v_pk_add_f32 v[18:19], v[18:19], 1.0 op_sel_hi:[1,0]
	v_med3_f32 v10, v10, s48, v208
	v_pk_mul_f32 v[14:15], v[18:19], v[14:15]
	v_med3_f32 v18, v20, s49, v208
	v_med3_f32 v19, v21, s49, v208
	v_pk_mul_f32 v[20:21], v[24:25], v[26:27] op_sel:[1,0] op_sel_hi:[0,0]
	v_med3_f32 v11, v11, s48, v208
	v_pk_mul_f32 v[16:17], v[16:17], v[20:21]
	v_pk_mul_f32 v[20:21], v[10:11], s[18:19] op_sel_hi:[1,0]
	v_pk_add_f32 v[18:19], v[18:19], 1.0 op_sel_hi:[1,0]
	v_exp_f32_e32 v20, v20
	v_exp_f32_e32 v21, v21
	v_pk_fma_f32 v[12:13], v[72:73], s[16:17], v[220:221] op_sel_hi:[1,0,1]
	v_pk_mul_f32 v[16:17], v[18:19], v[16:17]
	v_med3_f32 v12, v12, s48, v208
	v_pk_add_f32 v[18:19], v[20:21], 1.0 op_sel_hi:[1,0]
	v_med3_f32 v13, v13, s48, v208
	v_mul_f32_e32 v20, v18, v19
	v_rcp_f32_e32 v20, v20
	v_pk_mul_f32 v[24:25], v[12:13], s[18:19] op_sel_hi:[1,0]
	v_pk_fma_f32 v[6:7], v[78:79], s[16:17], v[214:215] op_sel_hi:[1,0,1]
	v_exp_f32_e32 v24, v24
	v_exp_f32_e32 v25, v25
	v_pk_mul_f32 v[18:19], v[18:19], v[20:21] op_sel:[1,0] op_sel_hi:[0,0]
	v_pk_mul_f32 v[10:11], v[10:11], v[18:19]
	v_med3_f32 v6, v6, s49, v208
	v_pk_add_f32 v[18:19], v[24:25], 1.0 op_sel_hi:[1,0]
	v_med3_f32 v7, v7, s49, v208
	v_mul_f32_e32 v20, v18, v19
	v_rcp_f32_e32 v20, v20
	v_pk_add_f32 v[6:7], v[6:7], 1.0 op_sel_hi:[1,0]
	v_pk_fma_f32 v[8:9], v[80:81], s[16:17], v[216:217] op_sel_hi:[1,0,1]
	v_pk_mul_f32 v[6:7], v[6:7], v[10:11]
	v_pk_mul_f32 v[10:11], v[18:19], v[20:21] op_sel:[1,0] op_sel_hi:[0,0]
	v_mov_b32_e32 v18, v198
	v_mov_b32_e32 v19, v198
	v_cvt_pk_fp8_f32 v18, v14, v15
	v_cvt_pk_fp8_f32 v19, v6, v7
	v_med3_f32 v8, v8, s49, v208
	v_med3_f32 v9, v9, s49, v208
	v_pk_add_f32 v[8:9], v[8:9], 1.0 op_sel_hi:[1,0]
	v_pk_mul_f32 v[6:7], v[12:13], v[10:11]
	v_cvt_pk_fp8_f32 v18, v16, v17 op_sel:[0,0,1]
	v_pk_mul_f32 v[6:7], v[8:9], v[6:7]
	s_nop 0
	v_cvt_pk_fp8_f32 v19, v6, v7 op_sel:[0,0,1]
	v_add_co_u32_e32 v6, vcc, 0x2c000, v22
	s_nop 1
	v_addc_co_u32_e32 v7, vcc, 0, v23, vcc
	s_and_b64 vcc, exec, s[2:3]
	s_mov_b64 s[2:3], -1
	global_store_dwordx2 v[6:7], v[18:19], off
	s_cbranch_vccnz .LBB0_956
	s_andn2_b64 vcc, exec, s[10:11]
	s_mov_b64 s[22:23], s[8:9]
	s_mov_b64 s[24:25], s[20:21]
	s_cbranch_vccnz .LBB0_972
	s_lshl_b32 s2, s41, 3
	s_add_i32 s2, s2, s39
	s_ashr_i32 s3, s2, 31
	s_lshl_b64 s[2:3], s[2:3], 18
	s_add_u32 s22, s37, s2
	s_addc_u32 s23, s38, s3
	s_mov_b64 s[24:25], s[6:7]
.LBB0_972:
	s_andn2_b64 vcc, exec, s[10:11]
	s_cbranch_vccnz .Lmy_gvdone
	s_waitcnt vmcnt(8)
	v_lshlrev_b32_e32 v2, 8, v209
	v_lshlrev_b32_e32 v3, 8, v210
	v_lshlrev_b32_e32 v4, 8, v211
	v_lshlrev_b32_e32 v5, 8, v212
	v_and_b32_e32 v2, 0xfffffc00, v2
	v_and_b32_e32 v3, 0xfffffc00, v3
	v_and_b32_e32 v4, 0xfffffc00, v4
	v_and_b32_e32 v5, 0xfffffc00, v5
	v_add_u32_e32 v2, v2, v201
	v_add_u32_e32 v3, v3, v202
	v_add_u32_e32 v4, v4, v201
	v_add_u32_e32 v5, v5, v202
